# sel: all three next-triple DMA blocks issued right after the triple barrier (whole triple to land) instead of one per block head
# baseline (speedup 1.0000x reference)
; #define LAS __attribute__((address_space(3)))
; #define RING_BARRIER() do { asm volatile("s_waitcnt lgkmcnt(0)" ::: "memory"); __builtin_amdgcn_s_barrier(); asm volatile("" ::: "memory"); } while (0)
; __device__ __forceinline__ void ringS_dma(const RingSLane& R, const char* K8p, const char* VTp, LAS unsigned char* sb, int wave) {
;     __builtin_amdgcn_global_load_lds((const unsigned*)(K8p + R.so[0]), (LAS unsigned*)(sb + wave * 1024), 16, 0, 0);
;     __builtin_amdgcn_global_load_lds((const unsigned*)((wave == 0 ? K8p : VTp) + R.so[1]), (LAS unsigned*)(sb + (wave + 8) * 1024), 16, 0, 0);
;     if (wave <= 2) __builtin_amdgcn_global_load_lds((const unsigned*)(VTp + R.so[2]), (LAS unsigned*)(sb + (wave + 16) * 1024), 16, 0, 0);
; }
; template <bool DUMMY> __device__ __forceinline__ void sel_phase(Frame& F) {
;     ...
;         SEL_DMA3(cj, F.lds);
;         for (int p = 0; p < npair; ++p) {
;             u32x2 dnx = {0xffffffffu, 0u}; if (p + 1 < npair) dnx = PD[(p + 1) * 8 + F.wave];
;             asm volatile("s_waitcnt vmcnt(0)" ::: "memory"); RING_BARRIER();
;             const unsigned nj = (unsigned)__builtin_amdgcn_readfirstlane((int)dnx.x), nb = (unsigned)__builtin_amdgcn_readfirstlane((int)dnx.y);
;             if (p + 1 < npair && !(DUMMY && MK_EXP == 2)) { SEL_DMA3(nj, F.lds + ((p + 1) & 1) * 3 * SLOTS); }
.Lsel_dma_all:
	s_bitcmp1_b32 s99, s37
	s_cbranch_scc0 .Lsel_dma_next
	s_lshr_b32 s12, s60, s36
	s_and_b32 s12, s12, 0xff
	s_lshl_b32 s12, s12, 13
	s_add_u32 s44, s62, s12
	s_addc_u32 s45, s63, 0
	s_add_u32 s12, s64, s12
	s_addc_u32 s13, s65, 0
	s_mul_i32 s97, s37, 0x4c00
	s_add_i32 s97, s98, s97
	s_mov_b32 m0, s97
	s_and_b64 vcc, exec, s[16:17]
	global_load_lds_dwordx4 v102, s[44:45]
	s_cselect_b32 s45, s45, s13
	s_cselect_b32 s44, s44, s12
	s_add_i32 m0, s97, 0x2000
	s_and_b64 vcc, exec, s[10:11]
	global_load_lds_dwordx4 v106, s[44:45]
	s_cbranch_vccnz .Lsel_dma_next
	s_add_i32 m0, s97, 0x4000
	s_nop 0
	global_load_lds_dwordx4 v108, s[12:13]
.Lsel_dma_next:
	s_add_i32 s37, s37, 1
	s_add_i32 s36, s36, 8
	s_cmp_lt_u32 s37, 3
	s_cbranch_scc1 .Lsel_dma_all
	s_mov_b32 s36, 0
	s_mov_b32 s37, 0
	s_branch .LBB0_1799

; #define LAS __attribute__((address_space(3)))
; __device__ __forceinline__ unsigned lds_addr(const LAS void* p) { return (unsigned)(size_t)p; }
; #define RD16(dst, base, off) asm volatile("ds_read_b128 %0, %1 offset:%2" : "=&v"(dst) : "v"(base), "i"(off) : "memory")
; #define LGKM_W(n) asm volatile("s_waitcnt lgkmcnt(" #n ")" ::: "memory"); SBAR()
; #define PV8_RD(dt) do { RD8(f.a[dt][0], vb, (dt) * 16 * VT8ST); RD8(f.a[dt][1], vb, (dt) * 16 * VT8ST + 32); } while (0)
; __device__ __forceinline__ void qk8_tile_c(f32x4 (&s)[4], const GS8& g, const unsigned kb  , const float c0  ) {
;     i32x4a lo[4], hi[4];
;     RD16(lo[0], kb, 0); RD16(hi[0], kb, 16); RD16(lo[1], kb, 16 * K8ST); RD16(hi[1], kb, 16 * K8ST + 16);
;     RD16(lo[2], kb, 32 * K8ST); RD16(hi[2], kb, 32 * K8ST + 16); RD16(lo[3], kb, 48 * K8ST); RD16(hi[3], kb, 48 * K8ST + 16);
;     ...
;     LGKM_W(6); QK8_MM(0); LGKM_W(4); QK8_MM(1); LGKM_W(2); QK8_MM(2); LGKM_W(0); QK8_MM(3);
;     ...
; }
; __device__ __forceinline__ void pv8_issue(VT8Frag& f, const unsigned vb  ) {
;     ...
;     PV8_RD(0); PV8_RD(1); PV8_RD(2); PV8_RD(3); PV8_RD(4); PV8_RD(5); PV8_RD(6); PV8_RD(7);
; template <bool DUMMY> __device__ __forceinline__ void sel_phase(Frame& F) {
;     ...
;             for (int h = 0; h < 3; ++h) {
;                 if (h > 0 && ((cj >> (23 + h)) & 1u) == 0u) continue;
;                 const int jc = (int)((cj >> (8 * h)) & 0xffu);
;                 LAS unsigned char* sb = F.lds + (((p & 1) * 3) + h) * SLOTS;
;                 unsigned byte = (cb >> (8 * h)) & 0xffu;
;                 if (DUMMY && MK_EXP == 1) byte = 0u;
;                 const unsigned a0 = byte & 0xfu, a1 = byte >> 4;
;                 if (byte == 0u) continue;
;                 const bool selA = ((a0 >> (c >> 2)) & 1u) != 0u, selB = ((a1 >> (c >> 2)) & 1u) != 0u;
;                 const float NINF = -__builtin_inff();
;                 const int kb = jc * 64; const bool diag = (jc == cur); f32x4 s0[4], s1[4];
;                 const float bA = selA ? 0.f : NINF, bB = selB ? 0.f : NINF;
;                 if (a0 != 0u) {
;                     const float rf = sm8_ref(g0);
;                     VT8Frag vf; qk8_tile_c(s0, g0, lds_addr(sb) + (unsigned)klane, bA + (5.f - rf)); pv8_issue(vf, lds_addr(sb + K8TB) + (unsigned)vtlane);
;                     if (diag) mask_scores(s0, tokA, 0x40000000u, kb, kq);
;                     online_sm8(s0, g0, rf);
.LBB0_1799:
.Lsel_nodma:
	s_lshr_b32 s45, s67, s36
	s_and_b32 s97, s45, 0xff
	s_cbranch_scc0 .LBB0_1798
	ds_read_b128 v[84:87], v208 offset:0
	ds_read_b128 v[88:91], v208 offset:16
	ds_read_b128 v[92:95], v208 offset:0x900
	ds_read_b128 v[96:99], v208 offset:0x910
	ds_read_b128 v[118:121], v208 offset:0x1200
	ds_read_b128 v[122:125], v208 offset:0x1210
	s_and_b32 vcc_lo, s45, 15
	s_cbranch_scc0 .Lsel_g1_pre
	v_and_b32_e32 v18, s45, v154
	v_cmp_eq_u32_e32 vcc, 0, v18
	s_lshr_b32 s44, s66, s36
	s_and_b32 s44, s44, 0xff
	v_cndmask_b32_e32 v210, v216, v181, vcc
	v_mov_b32_e32 v211, v210
	v_mov_b32_e32 v212, v210
	v_mov_b32_e32 v213, v210
	ds_read_b128 v[126:129], v208 offset:0x1b00
	ds_read_b128 v[130:133], v208 offset:0x1b10
	s_waitcnt lgkmcnt(6)
	v_mfma_scale_f32_16x16x128_f8f6f4 v[84:87], v[84:91], v[0:7], v[210:213], v178, v177 op_sel_hi:[0,0,0]
	ds_read_b128 v[134:137], v207 offset:0
	ds_read_b128 v[138:141], v207 offset:0x500
	ds_read_b128 v[142:145], v207 offset:0xa00
	ds_read_b128 v[146:149], v207 offset:0xf00
	s_waitcnt lgkmcnt(8)
	v_mfma_scale_f32_16x16x128_f8f6f4 v[88:91], v[92:99], v[0:7], v[210:213], v178, v177 op_sel_hi:[0,0,0]
	s_waitcnt lgkmcnt(6)
	v_mfma_scale_f32_16x16x128_f8f6f4 v[92:95], v[118:125], v[0:7], v[210:213], v178, v177 op_sel_hi:[0,0,0]
	s_waitcnt lgkmcnt(4)
	v_mfma_scale_f32_16x16x128_f8f6f4 v[96:99], v[126:133], v[0:7], v[210:213], v178, v177 op_sel_hi:[0,0,0]
	ds_read_b128 v[118:121], v207 offset:0x1400
	ds_read_b128 v[122:125], v207 offset:0x1900
	ds_read_b128 v[126:129], v207 offset:0x1e00
	ds_read_b128 v[130:133], v207 offset:0x2300
	s_cmp_eq_u32 s44, s58
	s_cbranch_scc1 .Lsel_diag_g0
